# gemm_in: the epilogue stores of each workgroup's last tile are write-through (sc1) so the data written just before the grid barrier is not freshly dirty in L2 at the XCD leader's release write-back
# speedup vs baseline: 1.0033x; 1.0033x over previous
.LBB0_265:
	s_add_i32 s37, s37, 1
	s_mul_i32 s4, s37, s36
	s_mul_hi_u32 s5, s37, s79
	s_add_i32 s5, s5, s4
	s_mul_i32 s4, s37, s79
	s_add_u32 s14, s4, s22
	s_addc_u32 s15, s5, s27
	s_cmp_ge_u32 s14, 0x770
	s_cselect_b32 s101, 1, 0
	v_mov_b64_e32 v[2:3], 0x770
	v_cmp_lt_i64_e64 s[6:7], s[14:15], v[2:3]
	v_mov_b64_e32 v[2:3], 0x76f
	v_cmp_gt_i64_e64 s[4:5], s[14:15], v[2:3]
	s_and_b64 vcc, exec, s[4:5]
	s_cbranch_vccnz .LBB0_267
	s_ashr_i32 s12, s14, 31
	s_lshr_b32 s12, s12, 29
	s_add_i32 s12, s14, s12
	s_ashr_i32 s13, s12, 3
	s_and_b32 s12, s12, -8
	s_sub_i32 s12, s14, s12
	s_cmp_lt_i32 s12, 0
	s_movk_i32 s14, 0xef
	s_cselect_b32 s14, s14, 0xee
	s_mul_i32 s12, s14, s12
	s_add_i32 s12, s12, s13
	s_mul_hi_i32 s13, s12, 0x92492493
	s_add_i32 s13, s13, s12
	s_lshr_b32 s14, s13, 31
	s_ashr_i32 s13, s13, 6
	s_add_i32 s13, s13, s14
	s_lshl_b32 s14, s13, 3
	s_sub_i32 s15, 0x88, s14
	s_min_i32 s15, s15, 8
	s_abs_i32 s18, s15
	v_cvt_f32_u32_e32 v2, s18
	s_sub_i32 s20, 0, s18
	s_mulk_i32 s13, 0x70
	s_sub_i32 s13, s12, s13
	v_rcp_iflag_f32_e32 v2, v2
	s_abs_i32 s12, s13
	s_xor_b32 s19, s13, s15
	s_ashr_i32 s19, s19, 31
	v_mul_f32_e32 v2, 0x4f7ffffe, v2
	v_cvt_u32_f32_e32 v2, v2
	s_nop 0
	v_readfirstlane_b32 s21, v2
	s_mul_i32 s20, s20, s21
	s_mul_hi_u32 s20, s21, s20
	s_add_i32 s21, s21, s20
	s_mul_hi_u32 s20, s12, s21
	s_mul_i32 s21, s20, s18
	s_sub_i32 s12, s12, s21
	s_add_i32 s33, s20, 1
	s_sub_i32 s21, s12, s18
	s_cmp_ge_u32 s12, s18
	s_cselect_b32 s20, s33, s20
	s_cselect_b32 s12, s21, s12
	s_add_i32 s21, s20, 1
	s_cmp_ge_u32 s12, s18
	s_cselect_b32 s12, s21, s20
	s_xor_b32 s12, s12, s19
	s_sub_i32 s12, s12, s19
	s_mul_i32 s15, s12, s15
	s_sub_i32 s13, s13, s15
	s_add_i32 s38, s13, s14

.LBB0_268:
	s_add_u32 s18, s8, s16
	s_addc_u32 s19, s9, s17
	s_add_u32 s20, s18, 0x100
	s_addc_u32 s21, s19, 0
	s_add_u32 s33, s42, s16
	s_addc_u32 s45, s43, s17
	s_cmpk_eq_i32 s16, 0x700
	s_cselect_b64 s[46:47], -1, 0
	s_and_b64 s[18:19], s[46:47], exec
	s_cselect_b32 s21, s9, s21
	s_cselect_b32 s20, s8, s20
	s_cselect_b32 s19, s13, s45
	s_cselect_b32 s18, s41, s33
	s_add_i32 s33, 0, 0x10000
	v_add_u32_e32 v135, s33, v148
	ds_read_b128 v[156:159], v135
	ds_read_b128 v[160:163], v135 offset:1024
	ds_read_b128 v[172:175], v135 offset:2048
	ds_read_b128 v[176:179], v135 offset:3072
	s_and_b64 vcc, s[6:7], s[46:47]
	v_cndmask_b32_e32 v226, v134, v152, vcc
	v_cndmask_b32_e32 v164, v136, v153, vcc
	v_cndmask_b32_e32 v135, v138, v154, vcc
	v_cndmask_b32_e32 v137, v140, v155, vcc
	v_lshl_add_u64 v[212:213], v[144:145], 0, s[16:17]
	s_add_i32 m0, s28, 0xc000
	ds_read_b128 v[180:183], v151
	ds_read_b128 v[184:187], v151 offset:1024
	ds_read_b128 v[188:191], v151 offset:2048
	ds_read_b128 v[192:195], v151 offset:3072
	ds_read_b128 v[196:199], v151 offset:4096
	ds_read_b128 v[200:203], v151 offset:5120
	ds_read_b128 v[204:207], v151 offset:6144
	ds_read_b128 v[208:211], v151 offset:7168
	global_load_lds_dwordx4 v[212:213], off
	v_lshl_add_u64 v[212:213], v[142:143], 0, s[16:17]
	s_add_i32 m0, s28, 0xe000
	s_nop 0
	global_load_lds_dwordx4 v[212:213], off
	s_waitcnt lgkmcnt(8)
	s_barrier
	s_waitcnt lgkmcnt(0)
	s_setprio 1
	s_waitcnt lgkmcnt(0)
	v_mfma_f32_16x16x32_bf16 v[126:129], v[156:159], v[180:183], v[126:129]
	v_mfma_f32_16x16x32_bf16 v[122:125], v[172:175], v[180:183], v[122:125]
	v_mfma_f32_16x16x32_bf16 v[118:121], v[156:159], v[188:191], v[118:121]
	v_mfma_f32_16x16x32_bf16 v[110:113], v[172:175], v[188:191], v[110:113]
	v_mfma_f32_16x16x32_bf16 v[102:105], v[156:159], v[196:199], v[102:105]
	v_mfma_f32_16x16x32_bf16 v[94:97], v[172:175], v[196:199], v[94:97]
	v_mfma_f32_16x16x32_bf16 v[86:89], v[156:159], v[204:207], v[86:89]
	v_mfma_f32_16x16x32_bf16 v[78:81], v[172:175], v[204:207], v[78:81]
	v_mfma_f32_16x16x32_bf16 v[126:129], v[160:163], v[184:187], v[126:129]
	v_mfma_f32_16x16x32_bf16 v[122:125], v[176:179], v[184:187], v[122:125]
	v_mfma_f32_16x16x32_bf16 v[118:121], v[160:163], v[192:195], v[118:121]
	v_mfma_f32_16x16x32_bf16 v[110:113], v[176:179], v[192:195], v[110:113]
	v_mfma_f32_16x16x32_bf16 v[102:105], v[160:163], v[200:203], v[102:105]
	v_mfma_f32_16x16x32_bf16 v[94:97], v[176:179], v[200:203], v[94:97]
	v_mfma_f32_16x16x32_bf16 v[86:89], v[160:163], v[208:211], v[86:89]
	v_mfma_f32_16x16x32_bf16 v[78:81], v[176:179], v[208:211], v[78:81]
	s_setprio 0
	s_barrier
	s_add_i32 s45, 0, 0x14000
	s_add_i32 s33, s33, s26
	v_add_u32_e32 v139, s45, v148
	v_lshl_add_u64 v[242:243], s[18:19], 0, v[132:133]
	s_mov_b32 m0, s33
	ds_read_b128 v[212:215], v139
	ds_read_b128 v[230:233], v139 offset:1024
	ds_read_b128 v[234:237], v139 offset:2048
	ds_read_b128 v[238:241], v139 offset:3072
	global_load_lds_dwordx4 v[242:243], off
	v_lshl_add_u64 v[244:245], s[18:19], 0, v[130:131]
	s_add_i32 m0, s33, 0x2000
	s_nop 0
	global_load_lds_dwordx4 v[244:245], off
	s_barrier
	s_waitcnt lgkmcnt(0)
	s_setprio 1
	s_waitcnt lgkmcnt(0)
	v_mfma_f32_16x16x32_bf16 v[114:117], v[212:215], v[180:183], v[114:117]
	v_mfma_f32_16x16x32_bf16 v[106:109], v[234:237], v[180:183], v[106:109]
	v_mfma_f32_16x16x32_bf16 v[98:101], v[212:215], v[188:191], v[98:101]
	v_mfma_f32_16x16x32_bf16 v[90:93], v[234:237], v[188:191], v[90:93]
	v_mfma_f32_16x16x32_bf16 v[82:85], v[212:215], v[196:199], v[82:85]
	v_mfma_f32_16x16x32_bf16 v[74:77], v[234:237], v[196:199], v[74:77]
	v_mfma_f32_16x16x32_bf16 v[62:65], v[212:215], v[204:207], v[62:65]
	v_mfma_f32_16x16x32_bf16 v[58:61], v[234:237], v[204:207], v[58:61]
	v_mfma_f32_16x16x32_bf16 v[114:117], v[230:233], v[184:187], v[114:117]
	v_mfma_f32_16x16x32_bf16 v[106:109], v[238:241], v[184:187], v[106:109]
	v_mfma_f32_16x16x32_bf16 v[98:101], v[230:233], v[192:195], v[98:101]
	v_mfma_f32_16x16x32_bf16 v[90:93], v[238:241], v[192:195], v[90:93]
	v_mfma_f32_16x16x32_bf16 v[82:85], v[230:233], v[200:203], v[82:85]
	v_mfma_f32_16x16x32_bf16 v[74:77], v[238:241], v[200:203], v[74:77]
	v_mfma_f32_16x16x32_bf16 v[62:65], v[230:233], v[208:211], v[62:65]
	v_mfma_f32_16x16x32_bf16 v[58:61], v[238:241], v[208:211], v[58:61]
	s_setprio 0
	s_mov_b32 m0, s28
	s_barrier
	ds_read_b128 v[180:183], v151 offset:16384
	ds_read_b128 v[184:187], v151 offset:17408
	ds_read_b128 v[188:191], v151 offset:18432
	ds_read_b128 v[192:195], v151 offset:19456
	ds_read_b128 v[196:199], v151 offset:20480
	ds_read_b128 v[200:203], v151 offset:21504
	ds_read_b128 v[204:207], v151 offset:22528
	ds_read_b128 v[208:211], v151 offset:23552
	global_load_lds_dwordx4 v226, s[20:21]
	s_mov_b32 m0, s29
	v_mov_b32_e32 v165, v227
	global_load_lds_dwordx4 v164, s[20:21]
	s_barrier
	s_waitcnt lgkmcnt(0)
	v_lshl_add_u64 v[246:247], s[20:21], 0, v[226:227]
	v_lshl_add_u64 v[164:165], s[20:21], 0, v[164:165]
	s_setprio 1
	s_waitcnt lgkmcnt(0)
	v_mfma_f32_16x16x32_bf16 v[46:49], v[156:159], v[180:183], v[46:49]
	v_mfma_f32_16x16x32_bf16 v[34:37], v[172:175], v[180:183], v[34:37]
	v_mfma_f32_16x16x32_bf16 v[22:25], v[156:159], v[188:191], v[22:25]
	v_mfma_f32_16x16x32_bf16 v[18:21], v[172:175], v[188:191], v[18:21]
	v_mfma_f32_16x16x32_bf16 v[14:17], v[156:159], v[196:199], v[14:17]
	v_mfma_f32_16x16x32_bf16 v[10:13], v[172:175], v[196:199], v[10:13]
	v_mfma_f32_16x16x32_bf16 v[6:9], v[156:159], v[204:207], v[6:9]
	v_mfma_f32_16x16x32_bf16 v[2:5], v[172:175], v[204:207], v[2:5]
	v_mfma_f32_16x16x32_bf16 v[46:49], v[160:163], v[184:187], v[46:49]
	v_mfma_f32_16x16x32_bf16 v[34:37], v[176:179], v[184:187], v[34:37]
	v_mfma_f32_16x16x32_bf16 v[22:25], v[160:163], v[192:195], v[22:25]
	v_mfma_f32_16x16x32_bf16 v[18:21], v[176:179], v[192:195], v[18:21]
	v_mfma_f32_16x16x32_bf16 v[14:17], v[160:163], v[200:203], v[14:17]
	v_mfma_f32_16x16x32_bf16 v[10:13], v[176:179], v[200:203], v[10:13]
	v_mfma_f32_16x16x32_bf16 v[6:9], v[160:163], v[208:211], v[6:9]
	v_mfma_f32_16x16x32_bf16 v[2:5], v[176:179], v[208:211], v[2:5]
	s_setprio 0
	s_barrier
	s_add_u32 s46, s18, 0x40000
	s_addc_u32 s47, s19, 0
	s_add_i32 s33, s45, s26
	v_lshl_add_u64 v[156:157], s[46:47], 0, v[132:133]
	s_mov_b32 m0, s33
	s_nop 0
	global_load_lds_dwordx4 v[156:157], off
	v_lshl_add_u64 v[156:157], s[46:47], 0, v[130:131]
	s_add_i32 m0, s33, 0x2000
	s_nop 0
	global_load_lds_dwordx4 v[156:157], off
	s_waitcnt vmcnt(6)
	s_barrier
	s_setprio 1
	v_mfma_f32_16x16x32_bf16 v[70:73], v[212:215], v[180:183], v[70:73]
	v_mfma_f32_16x16x32_bf16 v[66:69], v[234:237], v[180:183], v[66:69]
	v_mfma_f32_16x16x32_bf16 v[54:57], v[212:215], v[188:191], v[54:57]
	v_mfma_f32_16x16x32_bf16 v[50:53], v[234:237], v[188:191], v[50:53]
	v_mfma_f32_16x16x32_bf16 v[42:45], v[212:215], v[196:199], v[42:45]
	v_mfma_f32_16x16x32_bf16 v[38:41], v[234:237], v[196:199], v[38:41]
	v_mfma_f32_16x16x32_bf16 v[30:33], v[212:215], v[204:207], v[30:33]
	v_mfma_f32_16x16x32_bf16 v[26:29], v[234:237], v[204:207], v[26:29]
	v_mfma_f32_16x16x32_bf16 v[70:73], v[230:233], v[184:187], v[70:73]
	v_mfma_f32_16x16x32_bf16 v[66:69], v[238:241], v[184:187], v[66:69]
	v_mfma_f32_16x16x32_bf16 v[54:57], v[230:233], v[192:195], v[54:57]
	v_mfma_f32_16x16x32_bf16 v[50:53], v[238:241], v[192:195], v[50:53]
	v_mfma_f32_16x16x32_bf16 v[42:45], v[230:233], v[200:203], v[42:45]
	v_mfma_f32_16x16x32_bf16 v[38:41], v[238:241], v[200:203], v[38:41]
	v_mfma_f32_16x16x32_bf16 v[30:33], v[230:233], v[208:211], v[30:33]
	v_mfma_f32_16x16x32_bf16 v[26:29], v[238:241], v[208:211], v[26:29]
	s_setprio 0
	s_add_i32 s33, 0, 0x18000
	v_add_u32_e32 v139, s33, v148
	s_barrier
	ds_read_b128 v[156:159], v139
	ds_read_b128 v[160:163], v139 offset:1024
	ds_read_b128 v[172:175], v139 offset:2048
	ds_read_b128 v[176:179], v139 offset:3072
	s_mov_b32 m0, s30
	ds_read_b128 v[180:183], v151 offset:32768
	ds_read_b128 v[184:187], v151 offset:33792
	ds_read_b128 v[188:191], v151 offset:34816
	ds_read_b128 v[192:195], v151 offset:35840
	ds_read_b128 v[196:199], v151 offset:36864
	ds_read_b128 v[200:203], v151 offset:37888
	ds_read_b128 v[204:207], v151 offset:38912
	ds_read_b128 v[208:211], v151 offset:39936
	global_load_lds_dwordx4 v135, s[20:21]
	s_mov_b32 m0, s31
	s_nop 0
	global_load_lds_dwordx4 v137, s[20:21]
	s_waitcnt lgkmcnt(8)
	s_barrier
	s_waitcnt lgkmcnt(0)
	s_setprio 1
	s_waitcnt lgkmcnt(0)
	v_mfma_f32_16x16x32_bf16 v[126:129], v[156:159], v[180:183], v[126:129]
	v_mfma_f32_16x16x32_bf16 v[122:125], v[172:175], v[180:183], v[122:125]
	v_mfma_f32_16x16x32_bf16 v[118:121], v[156:159], v[188:191], v[118:121]
	v_mfma_f32_16x16x32_bf16 v[110:113], v[172:175], v[188:191], v[110:113]
	v_mfma_f32_16x16x32_bf16 v[102:105], v[156:159], v[196:199], v[102:105]
	v_mfma_f32_16x16x32_bf16 v[94:97], v[172:175], v[196:199], v[94:97]
	v_mfma_f32_16x16x32_bf16 v[86:89], v[156:159], v[204:207], v[86:89]
	v_mfma_f32_16x16x32_bf16 v[78:81], v[172:175], v[204:207], v[78:81]
	v_mfma_f32_16x16x32_bf16 v[126:129], v[160:163], v[184:187], v[126:129]
	v_mfma_f32_16x16x32_bf16 v[122:125], v[176:179], v[184:187], v[122:125]
	v_mfma_f32_16x16x32_bf16 v[118:121], v[160:163], v[192:195], v[118:121]
	v_mfma_f32_16x16x32_bf16 v[110:113], v[176:179], v[192:195], v[110:113]
	v_mfma_f32_16x16x32_bf16 v[102:105], v[160:163], v[200:203], v[102:105]
	v_mfma_f32_16x16x32_bf16 v[94:97], v[176:179], v[200:203], v[94:97]
	v_mfma_f32_16x16x32_bf16 v[86:89], v[160:163], v[208:211], v[86:89]
	v_mfma_f32_16x16x32_bf16 v[78:81], v[176:179], v[208:211], v[78:81]
	s_setprio 0
	s_barrier
	s_add_i32 s20, 0, 0x1c000
	s_add_i32 s21, s33, s26
	v_add_u32_e32 v135, s20, v148
	v_lshl_add_u64 v[242:243], v[242:243], 0, s[96:97]
	s_mov_b32 m0, s21
	ds_read_b128 v[212:215], v135
	ds_read_b128 v[230:233], v135 offset:1024
	ds_read_b128 v[234:237], v135 offset:2048
	ds_read_b128 v[238:241], v135 offset:3072
	global_load_lds_dwordx4 v[242:243], off
	v_lshl_add_u64 v[242:243], v[244:245], 0, s[96:97]
	s_add_i32 m0, s21, 0x2000
	s_nop 0
	global_load_lds_dwordx4 v[242:243], off
	s_barrier
	s_waitcnt lgkmcnt(0)
	s_setprio 1
	s_waitcnt lgkmcnt(0)
	v_mfma_f32_16x16x32_bf16 v[114:117], v[212:215], v[180:183], v[114:117]
	v_mfma_f32_16x16x32_bf16 v[106:109], v[234:237], v[180:183], v[106:109]
	v_mfma_f32_16x16x32_bf16 v[98:101], v[212:215], v[188:191], v[98:101]
	v_mfma_f32_16x16x32_bf16 v[90:93], v[234:237], v[188:191], v[90:93]
	v_mfma_f32_16x16x32_bf16 v[82:85], v[212:215], v[196:199], v[82:85]
	v_mfma_f32_16x16x32_bf16 v[74:77], v[234:237], v[196:199], v[74:77]
	v_mfma_f32_16x16x32_bf16 v[62:65], v[212:215], v[204:207], v[62:65]
	v_mfma_f32_16x16x32_bf16 v[58:61], v[234:237], v[204:207], v[58:61]
	v_mfma_f32_16x16x32_bf16 v[114:117], v[230:233], v[184:187], v[114:117]
	v_mfma_f32_16x16x32_bf16 v[106:109], v[238:241], v[184:187], v[106:109]
	v_mfma_f32_16x16x32_bf16 v[98:101], v[230:233], v[192:195], v[98:101]
	v_mfma_f32_16x16x32_bf16 v[90:93], v[238:241], v[192:195], v[90:93]
	v_mfma_f32_16x16x32_bf16 v[82:85], v[230:233], v[200:203], v[82:85]
	v_mfma_f32_16x16x32_bf16 v[74:77], v[238:241], v[200:203], v[74:77]
	v_mfma_f32_16x16x32_bf16 v[62:65], v[230:233], v[208:211], v[62:65]
	v_mfma_f32_16x16x32_bf16 v[58:61], v[238:241], v[208:211], v[58:61]
	s_setprio 0
	s_mov_b32 m0, s34
	v_lshl_add_u64 v[242:243], v[246:247], 0, s[96:97]
	s_barrier
	ds_read_b128 v[180:183], v151 offset:49152
	ds_read_b128 v[184:187], v151 offset:50176
	ds_read_b128 v[188:191], v151 offset:51200
	ds_read_b128 v[192:195], v151 offset:52224
	ds_read_b128 v[196:199], v151 offset:53248
	ds_read_b128 v[200:203], v151 offset:54272
	ds_read_b128 v[204:207], v151 offset:55296
	ds_read_b128 v[208:211], v151 offset:56320
	global_load_lds_dwordx4 v[242:243], off
	v_lshl_add_u64 v[164:165], v[164:165], 0, s[96:97]
	s_mov_b32 m0, s35
	s_nop 0
	global_load_lds_dwordx4 v[164:165], off
	s_barrier
	s_waitcnt lgkmcnt(0)
	s_setprio 1
	s_waitcnt lgkmcnt(0)
	v_mfma_f32_16x16x32_bf16 v[46:49], v[156:159], v[180:183], v[46:49]
	v_mfma_f32_16x16x32_bf16 v[34:37], v[172:175], v[180:183], v[34:37]
	v_mfma_f32_16x16x32_bf16 v[22:25], v[156:159], v[188:191], v[22:25]
	v_mfma_f32_16x16x32_bf16 v[18:21], v[172:175], v[188:191], v[18:21]
	v_mfma_f32_16x16x32_bf16 v[14:17], v[156:159], v[196:199], v[14:17]
	v_mfma_f32_16x16x32_bf16 v[10:13], v[172:175], v[196:199], v[10:13]
	v_mfma_f32_16x16x32_bf16 v[6:9], v[156:159], v[204:207], v[6:9]
	v_mfma_f32_16x16x32_bf16 v[2:5], v[172:175], v[204:207], v[2:5]
	v_mfma_f32_16x16x32_bf16 v[46:49], v[160:163], v[184:187], v[46:49]
	v_mfma_f32_16x16x32_bf16 v[34:37], v[176:179], v[184:187], v[34:37]
	v_mfma_f32_16x16x32_bf16 v[22:25], v[160:163], v[192:195], v[22:25]
	v_mfma_f32_16x16x32_bf16 v[18:21], v[176:179], v[192:195], v[18:21]
	v_mfma_f32_16x16x32_bf16 v[14:17], v[160:163], v[200:203], v[14:17]
	v_mfma_f32_16x16x32_bf16 v[10:13], v[176:179], v[200:203], v[10:13]
	v_mfma_f32_16x16x32_bf16 v[6:9], v[160:163], v[208:211], v[6:9]
	v_mfma_f32_16x16x32_bf16 v[2:5], v[176:179], v[208:211], v[2:5]
	s_setprio 0
	s_barrier
	s_add_u32 s18, s18, 0x40080
	s_addc_u32 s19, s19, 0
	s_add_i32 s20, s20, s26
	v_lshl_add_u64 v[156:157], s[18:19], 0, v[132:133]
	s_mov_b32 m0, s20
	s_nop 0
	global_load_lds_dwordx4 v[156:157], off
	v_lshl_add_u64 v[156:157], s[18:19], 0, v[130:131]
	s_add_i32 m0, s20, 0x2000
	s_nop 0
	global_load_lds_dwordx4 v[156:157], off
	s_waitcnt vmcnt(6)
	s_barrier
	s_setprio 1
	v_mfma_f32_16x16x32_bf16 v[70:73], v[212:215], v[180:183], v[70:73]
	v_mfma_f32_16x16x32_bf16 v[66:69], v[234:237], v[180:183], v[66:69]
	v_mfma_f32_16x16x32_bf16 v[54:57], v[212:215], v[188:191], v[54:57]
	v_mfma_f32_16x16x32_bf16 v[50:53], v[234:237], v[188:191], v[50:53]
	v_mfma_f32_16x16x32_bf16 v[42:45], v[212:215], v[196:199], v[42:45]
	v_mfma_f32_16x16x32_bf16 v[38:41], v[234:237], v[196:199], v[38:41]
	v_mfma_f32_16x16x32_bf16 v[30:33], v[212:215], v[204:207], v[30:33]
	v_mfma_f32_16x16x32_bf16 v[26:29], v[234:237], v[204:207], v[26:29]
	v_mfma_f32_16x16x32_bf16 v[70:73], v[230:233], v[184:187], v[70:73]
	v_mfma_f32_16x16x32_bf16 v[66:69], v[238:241], v[184:187], v[66:69]
	v_mfma_f32_16x16x32_bf16 v[54:57], v[230:233], v[192:195], v[54:57]
	v_mfma_f32_16x16x32_bf16 v[50:53], v[238:241], v[192:195], v[50:53]
	v_mfma_f32_16x16x32_bf16 v[42:45], v[230:233], v[200:203], v[42:45]
	v_mfma_f32_16x16x32_bf16 v[38:41], v[238:241], v[200:203], v[38:41]
	v_mfma_f32_16x16x32_bf16 v[30:33], v[230:233], v[208:211], v[30:33]
	v_mfma_f32_16x16x32_bf16 v[26:29], v[238:241], v[208:211], v[26:29]
	s_setprio 0
	s_add_i32 s44, s44, 2
	s_add_u32 s16, s16, 0x100
	s_addc_u32 s17, s17, 0
	s_cmp_gt_u32 s44, 13
	s_barrier
	s_cbranch_scc0 .LBB0_268
	v_lshl_or_b32 v136, s40, 8, v150
	v_lshl_add_u32 v140, s39, 8, v147
	v_ashrrev_i32_e32 v137, 31, v136
	v_mov_b64_e32 v[134:135], s[10:11]
	s_movk_i32 s13, 0x1c00
	v_mad_i64_i32 v[138:139], s[6:7], v140, s13, v[134:135]
	v_lshlrev_b64 v[136:137], 1, v[136:137]
	v_lshl_add_u64 v[138:139], v[138:139], 0, v[136:137]
	v_cvt_pk_bf16_f32 v126, v126, v127
	v_cvt_pk_bf16_f32 v127, v128, v129
	v_cvt_pk_bf16_f32 v128, v122, v123
	v_cvt_pk_bf16_f32 v129, v124, v125
	s_cmp_eq_u32 s101, 1
	s_cbranch_scc1 .Lgs_a_0
	global_store_dwordx4 v[138:139], v[126:129], off
	s_branch .Lgs_b_0
.Lgs_a_0:
	global_store_dwordx4 v[138:139], v[126:129], off sc1
.Lgs_b_0:
	v_cvt_pk_bf16_f32 v114, v114, v115
	v_cvt_pk_bf16_f32 v115, v116, v117
	v_cvt_pk_bf16_f32 v116, v106, v107
	v_or_b32_e32 v106, 16, v140
	v_mad_i64_i32 v[106:107], s[6:7], v106, s13, v[134:135]
	v_cvt_pk_bf16_f32 v117, v108, v109
	s_cmp_eq_u32 s101, 1
	s_cbranch_scc1 .Lgs_a_1
	global_store_dwordx4 v[138:139], v[114:117], off offset:256
	s_branch .Lgs_b_1
.Lgs_a_1:
	global_store_dwordx4 v[138:139], v[114:117], off offset:256 sc1
.Lgs_b_1:
	s_and_b64 vcc, exec, s[4:5]
	v_mov_b32_e32 v138, v154
	v_lshl_add_u64 v[114:115], v[106:107], 0, v[136:137]
	v_cvt_pk_bf16_f32 v106, v118, v119
	v_cvt_pk_bf16_f32 v107, v120, v121
	v_cvt_pk_bf16_f32 v108, v110, v111
	v_cvt_pk_bf16_f32 v109, v112, v113
	s_cmp_eq_u32 s101, 1
	s_cbranch_scc1 .Lgs_a_2
	global_store_dwordx4 v[114:115], v[106:109], off
	s_branch .Lgs_b_2
.Lgs_a_2:
	global_store_dwordx4 v[114:115], v[106:109], off sc1
.Lgs_b_2:
	v_cvt_pk_bf16_f32 v98, v98, v99
	v_cvt_pk_bf16_f32 v99, v100, v101
	v_cvt_pk_bf16_f32 v100, v90, v91
	v_or_b32_e32 v90, 32, v140
	v_mad_i64_i32 v[90:91], s[6:7], v90, s13, v[134:135]
	v_cvt_pk_bf16_f32 v101, v92, v93
	s_cmp_eq_u32 s101, 1
	s_cbranch_scc1 .Lgs_a_3
	global_store_dwordx4 v[114:115], v[98:101], off offset:256
	s_branch .Lgs_b_3
.Lgs_a_3:
	global_store_dwordx4 v[114:115], v[98:101], off offset:256 sc1
.Lgs_b_3:
	s_mov_b32 s40, s12
	s_mov_b32 s39, s38
	v_lshl_add_u64 v[98:99], v[90:91], 0, v[136:137]
	v_cvt_pk_bf16_f32 v90, v102, v103
	v_cvt_pk_bf16_f32 v91, v104, v105
	v_cvt_pk_bf16_f32 v92, v94, v95
	v_cvt_pk_bf16_f32 v93, v96, v97
	s_cmp_eq_u32 s101, 1
	s_cbranch_scc1 .Lgs_a_4
	global_store_dwordx4 v[98:99], v[90:93], off
	s_branch .Lgs_b_4
.Lgs_a_4:
	global_store_dwordx4 v[98:99], v[90:93], off sc1
.Lgs_b_4:
	v_cvt_pk_bf16_f32 v82, v82, v83
	v_cvt_pk_bf16_f32 v83, v84, v85
	v_cvt_pk_bf16_f32 v84, v74, v75
	v_or_b32_e32 v74, 48, v140
	v_mad_i64_i32 v[74:75], s[6:7], v74, s13, v[134:135]
	v_cvt_pk_bf16_f32 v85, v76, v77
	s_cmp_eq_u32 s101, 1
	s_cbranch_scc1 .Lgs_a_5
	global_store_dwordx4 v[98:99], v[82:85], off offset:256
	s_branch .Lgs_b_5
.Lgs_a_5:
	global_store_dwordx4 v[98:99], v[82:85], off offset:256 sc1
.Lgs_b_5:
	s_mov_b64 s[16:17], s[14:15]
	s_nop 0
	v_lshl_add_u64 v[82:83], v[74:75], 0, v[136:137]
	v_cvt_pk_bf16_f32 v74, v86, v87
	v_cvt_pk_bf16_f32 v75, v88, v89
	v_cvt_pk_bf16_f32 v76, v78, v79
	v_cvt_pk_bf16_f32 v77, v80, v81
	s_cmp_eq_u32 s101, 1
	s_cbranch_scc1 .Lgs_a_6
	global_store_dwordx4 v[82:83], v[74:77], off
	s_branch .Lgs_b_6
.Lgs_a_6:
	global_store_dwordx4 v[82:83], v[74:77], off sc1
.Lgs_b_6:
	v_cvt_pk_bf16_f32 v62, v62, v63
	v_cvt_pk_bf16_f32 v63, v64, v65
	v_cvt_pk_bf16_f32 v64, v58, v59
	v_add_u32_e32 v58, 0x80, v140
	v_mad_i64_i32 v[58:59], s[6:7], v58, s13, v[134:135]
	v_lshl_add_u64 v[58:59], v[58:59], 0, v[136:137]
	v_cvt_pk_bf16_f32 v65, v60, v61
	s_cmp_eq_u32 s101, 1
	s_cbranch_scc1 .Lgs_a_7
	global_store_dwordx4 v[82:83], v[62:65], off offset:256
	s_branch .Lgs_b_7
.Lgs_a_7:
	global_store_dwordx4 v[82:83], v[62:65], off offset:256 sc1
.Lgs_b_7:
	v_cvt_pk_bf16_f32 v46, v46, v47
	v_cvt_pk_bf16_f32 v47, v48, v49
	v_cvt_pk_bf16_f32 v48, v34, v35
	v_cvt_pk_bf16_f32 v49, v36, v37
	s_cmp_eq_u32 s101, 1
	s_cbranch_scc1 .Lgs_a_8
	global_store_dwordx4 v[58:59], v[46:49], off
	s_branch .Lgs_b_8
.Lgs_a_8:
	global_store_dwordx4 v[58:59], v[46:49], off sc1
.Lgs_b_8:
	v_cvt_pk_bf16_f32 v34, v70, v71
	v_cvt_pk_bf16_f32 v35, v72, v73
	v_cvt_pk_bf16_f32 v36, v66, v67
	v_cvt_pk_bf16_f32 v37, v68, v69
	s_cmp_eq_u32 s101, 1
	s_cbranch_scc1 .Lgs_a_9
	global_store_dwordx4 v[58:59], v[34:37], off offset:256
	s_branch .Lgs_b_9
.Lgs_a_9:
	global_store_dwordx4 v[58:59], v[34:37], off offset:256 sc1
.Lgs_b_9:
	v_cvt_pk_bf16_f32 v22, v22, v23
	v_cvt_pk_bf16_f32 v23, v24, v25
	v_cvt_pk_bf16_f32 v24, v18, v19
	v_cvt_pk_bf16_f32 v25, v20, v21
	s_nop 1
	v_add_u32_e32 v34, 0x90, v140
	v_mad_i64_i32 v[34:35], s[6:7], v34, s13, v[134:135]
	v_lshl_add_u64 v[34:35], v[34:35], 0, v[136:137]
	s_cmp_eq_u32 s101, 1
	s_cbranch_scc1 .Lgs_a_10
	global_store_dwordx4 v[34:35], v[22:25], off
	s_branch .Lgs_b_10
.Lgs_a_10:
	global_store_dwordx4 v[34:35], v[22:25], off sc1
.Lgs_b_10:
	v_cvt_pk_bf16_f32 v18, v54, v55
	v_cvt_pk_bf16_f32 v19, v56, v57
	v_cvt_pk_bf16_f32 v20, v50, v51
	v_cvt_pk_bf16_f32 v21, v52, v53
	s_cmp_eq_u32 s101, 1
	s_cbranch_scc1 .Lgs_a_11
	global_store_dwordx4 v[34:35], v[18:21], off offset:256
	s_branch .Lgs_b_11
.Lgs_a_11:
	global_store_dwordx4 v[34:35], v[18:21], off offset:256 sc1
.Lgs_b_11:
	v_cvt_pk_bf16_f32 v14, v14, v15
	v_cvt_pk_bf16_f32 v15, v16, v17
	v_cvt_pk_bf16_f32 v16, v10, v11
	v_cvt_pk_bf16_f32 v17, v12, v13
	s_nop 1
	v_add_u32_e32 v18, 0xa0, v140
	v_mad_i64_i32 v[18:19], s[6:7], v18, s13, v[134:135]
	v_lshl_add_u64 v[18:19], v[18:19], 0, v[136:137]
	s_cmp_eq_u32 s101, 1
	s_cbranch_scc1 .Lgs_a_12
	global_store_dwordx4 v[18:19], v[14:17], off
	s_branch .Lgs_b_12
.Lgs_a_12:
	global_store_dwordx4 v[18:19], v[14:17], off sc1
.Lgs_b_12:
	v_cvt_pk_bf16_f32 v10, v42, v43
	v_cvt_pk_bf16_f32 v11, v44, v45
	v_cvt_pk_bf16_f32 v12, v38, v39
	v_cvt_pk_bf16_f32 v13, v40, v41
	s_cmp_eq_u32 s101, 1
	s_cbranch_scc1 .Lgs_a_13
	global_store_dwordx4 v[18:19], v[10:13], off offset:256
	s_branch .Lgs_b_13
.Lgs_a_13:
	global_store_dwordx4 v[18:19], v[10:13], off offset:256 sc1
.Lgs_b_13:
	v_cvt_pk_bf16_f32 v6, v6, v7
	v_cvt_pk_bf16_f32 v7, v8, v9
	v_cvt_pk_bf16_f32 v8, v2, v3
	v_cvt_pk_bf16_f32 v9, v4, v5
	s_nop 1
	v_add_u32_e32 v10, 0xb0, v140
	v_mad_i64_i32 v[10:11], s[6:7], v10, s13, v[134:135]
	v_lshl_add_u64 v[10:11], v[10:11], 0, v[136:137]
	v_mov_b32_e32 v140, v155
	v_mov_b32_e32 v136, v153
	v_mov_b32_e32 v134, v152
	s_cmp_eq_u32 s101, 1
	s_cbranch_scc1 .Lgs_a_14
	global_store_dwordx4 v[10:11], v[6:9], off
	s_branch .Lgs_b_14
.Lgs_a_14:
	global_store_dwordx4 v[10:11], v[6:9], off sc1
.Lgs_b_14:
	v_cvt_pk_bf16_f32 v2, v30, v31
	v_cvt_pk_bf16_f32 v3, v32, v33
	v_cvt_pk_bf16_f32 v4, v26, v27
	v_cvt_pk_bf16_f32 v5, v28, v29
	s_cmp_eq_u32 s101, 1
	s_cbranch_scc1 .Lgs_a_15
	global_store_dwordx4 v[10:11], v[2:5], off offset:256
	s_branch .Lgs_b_15
.Lgs_a_15:
	global_store_dwordx4 v[10:11], v[2:5], off offset:256 sc1
